# attention: K-ring DMA issue between the 4th and 5th P.V MFMA, V-ring DMA behind the 8th, row-max under the P.V MFMAs (on v11)
# speedup vs baseline: 1.0088x; 1.0088x over previous
; #define ATT_DMAK(tile, slot) do { _Pragma("unroll") for (int i = 0; i < 4; ++i) { const int pc = (wv + 8 * i) < 25 ? (wv + 8 * i) : 24; \
;         __builtin_amdgcn_global_load_lds((const unsigned*)((const char*)Kbh + (size_t)(tile) * (64 * 384) + doffK[i]), (LAS unsigned*)(lds + (slot) * KT_BYTES + pc * 1024), 16, 0, 0); } } while (0)
; #define ATT_DMAV(tile, slot) do { _Pragma("unroll") for (int i = 0; i < 3; ++i) { const int pc = (wv + 8 * i) < 18 ? (wv + 8 * i) : 17; \
;         __builtin_amdgcn_global_load_lds((const unsigned*)((const char*)Vbh + (size_t)(tile) * 128 + doffV[i]), (LAS unsigned*)(lds + VRING + (slot) * VT_BYTES + pc * 1024), 16, 0, 0); } } while (0)
; __device__ __forceinline__ void attn_unit(const bf16_t* Qrows  , const bf16_t* Kbh, const bf16_t* Vbh, int nkeys, bf16_t* Orows, LAS unsigned char* lds) {
;     ...
;         if (j + 4 < nt) ATT_DMAK(j + 4, v0);
;         if (j + 3 < nt) ATT_DMAV(j + 3, v0 == 0 ? 2 : v0 - 1);
.LBB0_1235:
	s_add_i32 s15, s14, 1
	s_cmp_lg_u32 s14, 2
	s_cselect_b32 s14, s15, 0
	s_mul_i32 s15, s14, 0x6400
	v_add_u32_e32 v70, s15, v185
	ds_read_b128 v[66:69], v70
	ds_read_b128 v[166:169], v70 offset:32
	ds_read_b128 v[170:173], v70 offset:64
	ds_read_b128 v[188:191], v70 offset:96
	ds_read_b128 v[192:195], v70 offset:128
	ds_read_b128 v[196:199], v70 offset:160
	ds_read_b128 v[200:203], v70 offset:192
	ds_read_b128 v[216:219], v70 offset:224
	ds_read_b128 v[220:223], v70 offset:256
	ds_read_b128 v[224:227], v70 offset:288
	ds_read_b128 v[228:231], v70 offset:320
	ds_read_b128 v[146:149], v70 offset:352
	s_waitcnt lgkmcnt(11)
	v_mfma_f32_32x32x16_bf16 v[66:81], v[66:69], v[142:145], 0
	v_sub_f32_e32 v82, v82, v183
	v_exp_f32_e32 v82, v82
	v_sub_f32_e32 v94, v94, v183
	v_exp_f32_e32 v94, v94
	v_add_f32_e32 v165, 0, v82
	v_add_f32_e32 v165, v94, v165
	s_waitcnt lgkmcnt(10)
	v_mfma_f32_32x32x16_bf16 v[66:81], v[166:169], v[138:141], v[66:81]
	v_sub_f32_e32 v83, v83, v183
	v_exp_f32_e32 v83, v83
	v_sub_f32_e32 v95, v95, v183
	v_exp_f32_e32 v95, v95
	v_add_f32_e32 v165, v83, v165
	v_cvt_pk_bf16_f32 v82, v82, v83
	v_add_f32_e32 v165, v95, v165
	v_sub_f32_e32 v83, v84, v183
	s_waitcnt lgkmcnt(9)
	v_mfma_f32_32x32x16_bf16 v[66:81], v[170:173], v[134:137], v[66:81]
	v_exp_f32_e32 v83, v83
	v_sub_f32_e32 v96, v96, v183
	v_add_f32_e32 v84, v83, v165
	v_exp_f32_e32 v165, v96
	s_nop 0
	v_add_f32_e32 v84, v165, v84
	s_waitcnt lgkmcnt(8)
	v_mfma_f32_32x32x16_bf16 v[66:81], v[188:191], v[130:133], v[66:81]
	v_sub_f32_e32 v85, v85, v183
	v_exp_f32_e32 v85, v85
	v_sub_f32_e32 v96, v97, v183
	v_exp_f32_e32 v97, v96
	v_cvt_pk_bf16_f32 v96, v94, v95
	v_add_f32_e32 v84, v85, v84
	v_cvt_pk_bf16_f32 v83, v83, v85
	v_add_f32_e32 v84, v97, v84
	v_cvt_pk_bf16_f32 v97, v165, v97
	s_waitcnt lgkmcnt(7)
	v_mfma_f32_32x32x16_bf16 v[66:81], v[192:195], v[126:129], v[66:81]
	v_sub_f32_e32 v85, v86, v183
	v_exp_f32_e32 v85, v85
	s_nop 0
	v_add_f32_e32 v84, v85, v84
	s_waitcnt lgkmcnt(6)
	v_mfma_f32_32x32x16_bf16 v[66:81], v[196:199], v[122:125], v[66:81]
	v_sub_f32_e32 v86, v87, v183
	v_exp_f32_e32 v86, v86
	s_nop 0
	v_add_f32_e32 v87, v86, v84
	v_cvt_pk_bf16_f32 v84, v85, v86
	s_waitcnt lgkmcnt(5)
	v_mfma_f32_32x32x16_bf16 v[66:81], v[200:203], v[118:121], v[66:81]
	v_sub_f32_e32 v85, v88, v183
	v_exp_f32_e32 v85, v85
	s_nop 0
	v_add_f32_e32 v86, v85, v87
	s_waitcnt lgkmcnt(4)
	v_mfma_f32_32x32x16_bf16 v[66:81], v[216:219], v[114:117], v[66:81]
	v_sub_f32_e32 v87, v89, v183
	v_exp_f32_e32 v87, v87
	s_nop 0
	v_add_f32_e32 v86, v87, v86
	v_cvt_pk_bf16_f32 v85, v85, v87
	v_sub_f32_e32 v87, v90, v183
	v_exp_f32_e32 v90, v87
	s_waitcnt lgkmcnt(3)
	v_mfma_f32_32x32x16_bf16 v[66:81], v[220:223], v[110:113], v[66:81]
	v_add_u32_e32 v165, s13, v187
	v_add_f32_e32 v94, v90, v86
	ds_read_b128 v[86:89], v165
	ds_read_b128 v[166:169], v165 offset:32
	s_waitcnt lgkmcnt(4)
	v_mfma_f32_32x32x16_bf16 v[66:81], v[224:227], v[106:109], v[66:81]
	v_sub_f32_e32 v91, v91, v183
	ds_read_b128 v[170:173], v165 offset:4608
	ds_read_b128 v[188:191], v165 offset:4640
	v_exp_f32_e32 v91, v91
	s_nop 0
	v_add_f32_e32 v95, v91, v94
	v_cvt_pk_bf16_f32 v94, v90, v91
	s_waitcnt lgkmcnt(5)
	v_mfma_f32_32x32x16_bf16 v[66:81], v[228:231], v[102:105], v[66:81]
	v_sub_f32_e32 v90, v92, v183
	ds_read_b128 v[192:195], v165 offset:9216
	ds_read_b128 v[196:199], v165 offset:9248
	v_exp_f32_e32 v90, v90
	s_nop 0
	v_add_f32_e32 v91, v90, v95
	v_sub_f32_e32 v92, v93, v183
	v_exp_f32_e32 v92, v92
	s_waitcnt lgkmcnt(6)
	v_mfma_f32_32x32x16_bf16 v[66:81], v[146:149], v[98:101], v[66:81]
	v_add_f32_e32 v186, v92, v91
	v_cvt_pk_bf16_f32 v95, v90, v92
	ds_read_b128 v[90:93], v165 offset:13824
	ds_read_b128 v[146:149], v165 offset:13856
	s_waitcnt lgkmcnt(0)
	v_mfma_f32_32x32x16_bf16 v[50:65], v[86:89], v[82:85], v[50:65]
	v_add_f32_e32 v186, v164, v186
	v_mfma_f32_32x32x16_bf16 v[34:49], v[170:173], v[82:85], v[34:49]
	v_mfma_f32_32x32x16_bf16 v[18:33], v[192:195], v[82:85], v[18:33]
	v_max_f32_e32 v150, v66, v67
	v_max3_f32 v150, v150, v68, v69
	v_mfma_f32_32x32x16_bf16 v[2:17], v[90:93], v[82:85], v[2:17]
	s_and_b64 vcc, exec, s[0:1]
	s_cbranch_vccnz .LattB_v
	s_mul_i32 s13, s12, 0x6400
	s_add_i32 s13, s13, 0
	s_add_u32 s16, s80, s2
	s_addc_u32 s17, s81, s3
	s_add_u32 s16, s16, 0x30e90000
	s_addc_u32 s17, s17, 0
	s_add_i32 m0, s13, s65
	s_nop 0
	global_load_lds_dwordx4 v208, s[16:17]
	s_add_i32 m0, s13, s66
	s_nop 0
	global_load_lds_dwordx4 v209, s[16:17]
	s_add_i32 m0, s13, s67
	s_add_i32 s13, s13, s68
	global_load_lds_dwordx4 v210, s[16:17]
	s_add_i32 m0, s13, 0x6000
	s_nop 0
	global_load_lds_dwordx4 v211, s[16:17]
.LattB_v:
	v_max3_f32 v150, v150, v70, v71
	v_max3_f32 v150, v150, v72, v73
	v_mfma_f32_32x32x16_bf16 v[50:65], v[166:169], v[94:97], v[50:65]
	v_max3_f32 v150, v150, v74, v75
	v_max3_f32 v150, v150, v76, v77
	v_mfma_f32_32x32x16_bf16 v[34:49], v[188:191], v[94:97], v[34:49]
	v_max3_f32 v150, v150, v78, v79
	v_max3_f32 v150, v150, v80, v81
	v_mfma_f32_32x32x16_bf16 v[18:33], v[196:199], v[94:97], v[18:33]
	v_mfma_f32_32x32x16_bf16 v[2:17], v[146:149], v[94:97], v[2:17]
	v_mov_b32_e32 v151, v150
	s_nop 1
	v_permlane32_swap_b32_e32 v151, v150
	v_max_f32_e32 v150, v150, v151
	s_andn2_b64 vcc, exec, s[24:25]
	s_mul_i32 s13, s12, 0x4800
	s_cbranch_vccnz .LattB_end
	s_add_i32 s15, s13, 0xffffb800
	s_cmp_lg_u32 s12, 0
	s_cselect_b32 s15, s15, 0x9000
	s_add_i32 s15, s15, 0
	s_add_i32 s15, s15, 0x12c00
	s_add_u32 s16, s82, s2
	s_addc_u32 s17, s83, s3
	s_add_u32 s16, s16, 0x31bf8180
	s_addc_u32 s17, s17, 0
	s_add_i32 m0, s15, s69
	s_nop 0
	global_load_lds_dwordx4 v212, s[16:17]
	s_add_i32 m0, s15, s70
	s_nop 0
	global_load_lds_dwordx4 v213, s[16:17]
	s_add_i32 m0, s15, s71
	s_nop 0
	global_load_lds_dwordx4 v214, s[16:17]

; #define ATT_DMAK(tile, slot) do { _Pragma("unroll") for (int i = 0; i < 4; ++i) { const int pc = (wv + 8 * i) < 25 ? (wv + 8 * i) : 24; \
;         __builtin_amdgcn_global_load_lds((const unsigned*)((const char*)Kbh + (size_t)(tile) * (64 * 384) + doffK[i]), (LAS unsigned*)(lds + (slot) * KT_BYTES + pc * 1024), 16, 0, 0); } } while (0)
; #define ATT_DMAV(tile, slot) do { _Pragma("unroll") for (int i = 0; i < 3; ++i) { const int pc = (wv + 8 * i) < 18 ? (wv + 8 * i) : 17; \
;         __builtin_amdgcn_global_load_lds((const unsigned*)((const char*)Vbh + (size_t)(tile) * 128 + doffV[i]), (LAS unsigned*)(lds + VRING + (slot) * VT_BYTES + pc * 1024), 16, 0, 0); } } while (0)
; __device__ __forceinline__ void attn_unit(const bf16_t* Qrows  , const bf16_t* Kbh, const bf16_t* Vbh, int nkeys, bf16_t* Orows, LAS unsigned char* lds) {
;     ...
;         if (j + 3 < nt) ATT_DMAK(j + 3, v0);
;         ATT_DMAV(j + 2, v0 == 0 ? 2 : v0 - 1);
.LBB0_1240:
	s_mul_i32 s13, s14, 0x6400
	v_add_u32_e32 v86, s13, v185
	ds_read_b128 v[82:85], v86
	ds_read_b128 v[188:191], v86 offset:32
	ds_read_b128 v[192:195], v86 offset:64
	ds_read_b128 v[196:199], v86 offset:96
	ds_read_b128 v[200:203], v86 offset:128
	ds_read_b128 v[216:219], v86 offset:160
	ds_read_b128 v[220:223], v86 offset:192
	ds_read_b128 v[224:227], v86 offset:224
	ds_read_b128 v[228:231], v86 offset:256
	ds_read_b128 v[232:235], v86 offset:288
	ds_read_b128 v[236:239], v86 offset:320
	ds_read_b128 v[240:243], v86 offset:352
	s_waitcnt lgkmcnt(11)
	v_mfma_f32_32x32x16_bf16 v[82:97], v[82:85], v[142:145], 0
	v_sub_f32_e32 v66, v66, v183
	v_sub_f32_e32 v78, v78, v183
	v_exp_f32_e32 v66, v66
	v_exp_f32_e32 v78, v78
	s_waitcnt lgkmcnt(10)
	v_mfma_f32_32x32x16_bf16 v[82:97], v[188:191], v[138:141], v[82:97]
	v_sub_f32_e32 v67, v67, v183
	v_sub_f32_e32 v79, v79, v183
	v_exp_f32_e32 v67, v67
	v_exp_f32_e32 v79, v79
	v_cvt_pk_bf16_f32 v188, v66, v67
	s_waitcnt lgkmcnt(9)
	v_mfma_f32_32x32x16_bf16 v[82:97], v[192:195], v[134:137], v[82:97]
	v_sub_f32_e32 v68, v68, v183
	v_sub_f32_e32 v80, v80, v183
	v_exp_f32_e32 v68, v68
	v_exp_f32_e32 v80, v80
	s_waitcnt lgkmcnt(8)
	v_mfma_f32_32x32x16_bf16 v[82:97], v[196:199], v[130:133], v[82:97]
	v_sub_f32_e32 v69, v69, v183
	v_sub_f32_e32 v81, v81, v183
	v_exp_f32_e32 v69, v69
	v_exp_f32_e32 v81, v81
	v_cvt_pk_bf16_f32 v194, v78, v79
	v_cvt_pk_bf16_f32 v189, v68, v69
	v_cvt_pk_bf16_f32 v195, v80, v81
	s_waitcnt lgkmcnt(7)
	v_mfma_f32_32x32x16_bf16 v[82:97], v[200:203], v[126:129], v[82:97]
	v_sub_f32_e32 v70, v70, v183
	v_exp_f32_e32 v70, v70
	s_waitcnt lgkmcnt(6)
	v_mfma_f32_32x32x16_bf16 v[82:97], v[216:219], v[122:125], v[82:97]
	v_sub_f32_e32 v71, v71, v183
	v_exp_f32_e32 v71, v71
	s_nop 0
	v_cvt_pk_bf16_f32 v190, v70, v71
	s_waitcnt lgkmcnt(5)
	v_mfma_f32_32x32x16_bf16 v[82:97], v[220:223], v[118:121], v[82:97]
	v_sub_f32_e32 v72, v72, v183
	v_exp_f32_e32 v72, v72
	s_waitcnt lgkmcnt(4)
	v_mfma_f32_32x32x16_bf16 v[82:97], v[224:227], v[114:117], v[82:97]
	v_sub_f32_e32 v73, v73, v183
	v_exp_f32_e32 v73, v73
	s_nop 0
	v_cvt_pk_bf16_f32 v191, v72, v73
	s_waitcnt lgkmcnt(3)
	v_mfma_f32_32x32x16_bf16 v[82:97], v[228:231], v[110:113], v[82:97]
	v_add_u32_e32 v204, s12, v187
	v_sub_f32_e32 v74, v74, v183
	ds_read_b128 v[196:199], v204
	ds_read_b128 v[200:203], v204 offset:32
	v_exp_f32_e32 v74, v74
	s_waitcnt lgkmcnt(4)
	v_mfma_f32_32x32x16_bf16 v[82:97], v[232:235], v[106:109], v[82:97]
	v_sub_f32_e32 v75, v75, v183
	ds_read_b128 v[216:219], v204 offset:4608
	ds_read_b128 v[220:223], v204 offset:4640
	v_exp_f32_e32 v75, v75
	s_nop 0
	v_cvt_pk_bf16_f32 v192, v74, v75
	s_waitcnt lgkmcnt(5)
	v_mfma_f32_32x32x16_bf16 v[82:97], v[236:239], v[102:105], v[82:97]
	v_sub_f32_e32 v76, v76, v183
	ds_read_b128 v[224:227], v204 offset:9216
	ds_read_b128 v[228:231], v204 offset:9248
	v_exp_f32_e32 v76, v76
	s_waitcnt lgkmcnt(6)
	v_mfma_f32_32x32x16_bf16 v[82:97], v[240:243], v[98:101], v[82:97]
	v_sub_f32_e32 v77, v77, v183
	ds_read_b128 v[232:235], v204 offset:13824
	ds_read_b128 v[236:239], v204 offset:13856
	v_exp_f32_e32 v77, v77
	s_nop 0
	v_cvt_pk_bf16_f32 v193, v76, v77
	s_waitcnt lgkmcnt(0)
	v_mfma_f32_32x32x16_bf16 v[50:65], v[196:199], v[188:191], v[50:65]
	v_mfma_f32_32x32x16_bf16 v[34:49], v[216:219], v[188:191], v[34:49]
	v_mfma_f32_32x32x16_bf16 v[18:33], v[224:227], v[188:191], v[18:33]
	v_max_f32_e32 v152, v82, v83
	v_max3_f32 v152, v152, v84, v85
	v_mfma_f32_32x32x16_bf16 v[2:17], v[232:235], v[188:191], v[2:17]
	s_and_b64 vcc, exec, s[0:1]
	s_cbranch_vccnz .LattA_v
	s_mul_i32 s12, s36, 0x6400
	s_add_i32 s12, s12, 0
	s_add_u32 s16, s80, s2
	s_addc_u32 s17, s81, s3
	s_add_u32 s16, s16, 0x30e8a000
	s_addc_u32 s17, s17, 0
	s_add_i32 m0, s12, s65
	s_nop 0
	global_load_lds_dwordx4 v208, s[16:17]
	s_add_i32 m0, s12, s66
	s_nop 0
	global_load_lds_dwordx4 v209, s[16:17]
	s_add_i32 m0, s12, s67
	s_add_i32 s12, s12, s68
	global_load_lds_dwordx4 v210, s[16:17]
	s_add_i32 m0, s12, 0x6000
	s_nop 0
	global_load_lds_dwordx4 v211, s[16:17]
.LattA_v:
	v_max3_f32 v152, v152, v86, v87
	v_max3_f32 v152, v152, v88, v89
	v_mfma_f32_32x32x16_bf16 v[50:65], v[200:203], v[192:195], v[50:65]
	v_max3_f32 v152, v152, v90, v91
	v_max3_f32 v152, v152, v92, v93
	v_mfma_f32_32x32x16_bf16 v[34:49], v[220:223], v[192:195], v[34:49]
	v_max3_f32 v152, v152, v94, v95
	v_max3_f32 v152, v152, v96, v97
	v_mfma_f32_32x32x16_bf16 v[18:33], v[228:231], v[192:195], v[18:33]
	v_mfma_f32_32x32x16_bf16 v[2:17], v[236:239], v[192:195], v[2:17]
	v_mov_b32_e32 v153, v152
	s_nop 1
	v_permlane32_swap_b32_e32 v153, v152
	v_max_f32_e32 v152, v152, v153
	s_mul_i32 s12, s36, 0x4800
	s_add_i32 s13, s12, 0xffffb800
	s_cmp_lg_u32 s36, 0
	s_cselect_b32 s13, s13, 0x9000
	s_add_i32 s13, s13, 0
	s_add_i32 s13, s13, 0x12c00
	s_add_u32 s16, s82, s2
	s_addc_u32 s17, s83, s3
	s_add_u32 s16, s16, s28
	s_addc_u32 s17, s17, s29
	s_add_i32 m0, s13, s69
	s_nop 0
	global_load_lds_dwordx4 v212, s[16:17]
	s_add_i32 m0, s13, s70
	s_nop 0
	global_load_lds_dwordx4 v213, s[16:17]
	s_add_i32 m0, s13, s71
	s_nop 0
	global_load_lds_dwordx4 v214, s[16:17]
	s_mov_b64 s[12:13], -1
	s_and_b64 vcc, exec, s[0:1]
	s_cbranch_vccz .LBB0_1242
	s_waitcnt vmcnt(0)
	s_mov_b64 s[12:13], 0
